# speedup vs baseline: 1.0061x; 1.0061x over previous
.LBB3_61:
	s_or_b64 exec, exec, s[4:5]
	s_movk_i32 s5, 0x2b0
	v_mov_b32_e32 v5, 0x15000
	v_mad_u32_u24 v206, v0, s5, v5
	v_mov_b32_e32 v5, 0x3c00
	v_cmp_eq_u32_e32 vcc, 0, v55
	s_movk_i32 s4, 0xf0
	v_mul_u32_u24_e32 v3, 56, v55
	v_cndmask_b32_e32 v208, 0, v5, vcc
	v_lshlrev_b32_e32 v5, 3, v204
	v_lshl_or_b32 v5, v195, 8, v5
	v_add_u32_e32 v209, 0x26a80, v5
	v_mov_b32_e32 v5, 0x23800
	v_mov_b32_e32 v2, 0x1fc00
	v_mad_u32_u24 v4, v204, s5, v3
	s_mov_b32 s8, 0x15000
	v_mad_u32_u24 v207, v204, s4, v5
	v_lshlrev_b32_e32 v5, 3, v205
	v_lshlrev_b32_e32 v194, 4, v205
	v_mad_u32_u24 v2, v204, s4, v2
	v_add3_u32 v210, v207, v3, v5
	v_add3_u32 v212, v4, v194, s8
	s_movk_i32 s4, 0x64
	v_mov_b32_e32 v4, 0x25600
	v_mad_u32_u24 v214, v0, s4, v4
	v_add_u32_e32 v0, 48, v210
	v_cmp_gt_u32_e64 s[4:5], 32, v1
	v_add_u32_e32 v211, v2, v194
	v_add3_u32 v217, v2, v3, v5
	v_cndmask_b32_e64 v218, v209, v0, s[4:5]
	v_mul_u32_u24_e32 v0, 0x1c0, v195
	v_or_b32_e32 v0, v0, v1
	v_lshlrev_b32_e32 v0, 4, v0
	v_mov_b32_e32 v1, 0
	v_add_u32_e32 v2, 0x1000, v0
	v_mov_b32_e32 v3, v1
	v_lshl_add_u64 v[196:197], s[0:1], 0, v[0:1]
	v_lshl_add_u64 v[198:199], s[0:1], 0, v[2:3]
	v_add_u32_e32 v2, 0x1400, v0
	v_add_u32_e32 v0, 0x1800, v0
	v_add_u32_e32 v213, 0x26280, v50
	v_lshl_add_u32 v215, v54, 4, v50
	v_lshl_add_u64 v[200:201], s[0:1], 0, v[2:3]
	v_lshl_add_u64 v[202:203], s[0:1], 0, v[0:1]
	v_mov_b32_e32 v0, v1
	v_mov_b32_e32 v2, v1
	v_mov_b32_e32 v4, v1
	v_mov_b32_e32 v5, v1
	v_mov_b32_e32 v6, v1
	v_mov_b32_e32 v7, v1
	v_mov_b32_e32 v8, v1
	v_mov_b32_e32 v9, v1
	v_mov_b32_e32 v10, v1
	v_mov_b32_e32 v11, v1
	v_mov_b32_e32 v12, v1
	v_mov_b64_e32 v[80:81], v[14:15]
	v_mov_b64_e32 v[64:65], v[14:15]
	v_mov_b64_e32 v[48:49], v[14:15]
	s_mov_b32 s14, 0
	v_add_u32_e32 v216, v207, v194
	s_mov_b32 s15, 0x5040100
	s_movk_i32 s18, 0x2a0
	v_mov_b64_e32 v[78:79], v[12:13]
	v_mov_b64_e32 v[76:77], v[10:11]
	v_mov_b64_e32 v[74:75], v[8:9]
	v_mov_b64_e32 v[72:73], v[6:7]
	v_mov_b64_e32 v[70:71], v[4:5]
	v_mov_b64_e32 v[68:69], v[2:3]
	v_mov_b64_e32 v[66:67], v[0:1]
	v_mov_b64_e32 v[62:63], v[12:13]
	v_mov_b64_e32 v[60:61], v[10:11]
	v_mov_b64_e32 v[58:59], v[8:9]
	v_mov_b64_e32 v[56:57], v[6:7]
	v_mov_b64_e32 v[54:55], v[4:5]
	v_mov_b64_e32 v[52:53], v[2:3]
	v_mov_b64_e32 v[50:51], v[0:1]
	v_mov_b64_e32 v[46:47], v[12:13]
	v_mov_b64_e32 v[44:45], v[10:11]
	v_mov_b64_e32 v[42:43], v[8:9]
	v_mov_b64_e32 v[40:41], v[6:7]
	v_mov_b64_e32 v[38:39], v[4:5]
	v_mov_b64_e32 v[36:37], v[2:3]
	v_mov_b64_e32 v[34:35], v[0:1]
	v_mov_b32_e32 v13, v1
	v_mov_b32_e32 v14, v1
	v_mov_b32_e32 v15, v1
	v_mov_b32_e32 v16, v1
	v_mov_b32_e32 v17, v1
	v_mov_b32_e32 v18, v1
	v_mov_b32_e32 v19, v1
	v_mov_b32_e32 v20, v1
	v_mov_b32_e32 v21, v1
	v_mov_b32_e32 v22, v1
	v_mov_b32_e32 v23, v1
	v_mov_b32_e32 v24, v1
	v_mov_b32_e32 v25, v1
	v_mov_b32_e32 v26, v1
	v_mov_b32_e32 v27, v1
	v_mov_b32_e32 v28, v1
	v_mov_b32_e32 v29, v1
	v_mov_b32_e32 v30, v1
	v_lshlrev_b32_e32 v240, 1, v192
	v_sub_u32_e32 v241, v190, v192
	v_lshlrev_b32_e32 v241, 1, v241
	v_add_u32_e32 v242, v206, v240
	v_lshl_add_u32 v243, v190, 1, v206
	s_cmp_eq_u32 s47, 2
	s_cbranch_scc1 .Lgru_restore
	s_cmp_lt_u32 s72, 0x100
	s_cbranch_scc1 .Lapf_skip_a
	ds_read_b128 v[232:235], v215
	ds_read_b128 v[236:239], v215 offset:7168
	ds_read_b128 v[240:243], v215 offset:14336
	ds_read_b128 v[244:247], v215 offset:1024
	ds_read_b128 v[200:203], v215 offset:8192

.LBB3_71:
	s_andn2_b64 vcc, exec, s[8:9]
	s_cbranch_vccnz .LBB3_73
	s_setprio 1
	ds_read_b128 v[64:67], v213
	s_mul_i32 s8, s20, 0x5600
	v_add_u32_e32 v0, s8, v212
	s_waitcnt vmcnt(6)
	ds_read2_b64 v[2:5], v0 offset1:1
	ds_read_b128 v[220:223], v213 offset:1024
	ds_read2_b64 v[34:37], v0 offset0:4 offset1:5
	s_waitcnt vmcnt(2)
	ds_read2_b64 v[18:21], v0 offset0:28 offset1:29
	ds_read2_b64 v[38:41], v0 offset0:32 offset1:33
	s_mul_i32 s8, s20, 0x1e00
	v_add_u32_e32 v63, s8, v211
	s_min_u32 s8, s14, 22
	s_waitcnt vmcnt(0) lgkmcnt(1)
	v_mfma_f32_32x32x16_f16 v[18:33], v[64:67], v[18:21], 0
	v_mfma_f32_32x32x16_f16 v[2:17], v[64:67], v[2:5], 0
	s_waitcnt lgkmcnt(0)
	v_mfma_f32_32x32x16_f16 v[18:33], v[220:223], v[38:41], v[18:33]
	v_mfma_f32_32x32x16_f16 v[2:17], v[220:223], v[34:37], v[2:17]
	ds_read_b128 v[34:37], v63
	ds_read_b128 v[68:71], v63 offset:32
	s_waitcnt lgkmcnt(1)
	v_mfma_f32_32x32x16_f16 v[18:33], v[130:133], v[34:37], v[18:33]
	v_mfma_f32_32x32x16_f16 v[2:17], v[82:85], v[34:37], v[2:17]
	v_mfma_f32_32x32x16_f16 v[34:49], v[138:141], v[34:37], 0
	s_waitcnt lgkmcnt(0)
	v_mfma_f32_32x32x16_f16 v[18:33], v[110:113], v[68:71], v[18:33]
	v_mfma_f32_32x32x16_f16 v[2:17], v[86:89], v[68:71], v[2:17]
	v_mfma_f32_32x32x16_f16 v[34:49], v[142:145], v[68:71], v[34:49]
	ds_read_b128 v[68:71], v63 offset:64
	ds_read_b128 v[72:75], v63 offset:96
	s_waitcnt lgkmcnt(1)
	v_mfma_f32_32x32x16_f16 v[18:33], v[114:117], v[68:71], v[18:33]
	v_mfma_f32_32x32x16_f16 v[2:17], v[90:93], v[68:71], v[2:17]
	v_mfma_f32_32x32x16_f16 v[34:49], v[146:149], v[68:71], v[34:49]
	s_waitcnt lgkmcnt(0)
	v_mfma_f32_32x32x16_f16 v[18:33], v[118:121], v[72:75], v[18:33]
	v_mfma_f32_32x32x16_f16 v[2:17], v[94:97], v[72:75], v[2:17]
	v_mfma_f32_32x32x16_f16 v[34:49], v[150:153], v[72:75], v[34:49]
	ds_read_b128 v[68:71], v63 offset:128
	ds_read_b128 v[72:75], v63 offset:160
	s_waitcnt lgkmcnt(1)
	v_mfma_f32_32x32x16_f16 v[18:33], v[122:125], v[68:71], v[18:33]
	s_waitcnt lgkmcnt(0)
	v_mfma_f32_32x32x16_f16 v[18:33], v[126:129], v[72:75], v[18:33]
	v_mfma_f32_32x32x16_f16 v[2:17], v[106:109], v[68:71], v[2:17]
	v_mfma_f32_32x32x16_f16 v[34:49], v[154:157], v[68:71], v[34:49]
	ds_read_b128 v[68:71], v63 offset:192
	v_lshl_add_u32 v63, s8, 2, v214
	ds_read_b32 v63, v63 offset:8
	s_mul_i32 s8, s19, 0x5600
	s_waitcnt lgkmcnt(1)
	v_mfma_f32_32x32x16_f16 v[18:33], v[134:137], v[68:71], v[18:33]
	v_mfma_f32_32x32x16_f16 v[2:17], v[98:101], v[72:75], v[2:17]
	v_mfma_f32_32x32x16_f16 v[34:49], v[158:161], v[72:75], v[34:49]
	ds_read2_b64 v[72:75], v0 offset0:56 offset1:57
	ds_read2_b64 v[224:227], v0 offset0:60 offset1:61
	s_waitcnt lgkmcnt(2)
	v_mad_u32_u24 v228, v63, s18, v240
	v_add_u32_e32 v31, s8, v242
	ds_write_b128 v31, v[178:181]
	ds_write_b128 v31, v[174:177] offset:128
	global_load_dwordx4 v[178:181], v228, s[10:11]
	global_load_dwordx4 v[174:177], v228, s[10:11] offset:128
	ds_write_b128 v31, v[170:173] offset:256
	ds_write_b128 v31, v[166:169] offset:384
	v_add_u32_e32 v0, s8, v243
	global_load_dwordx4 v[170:173], v228, s[10:11] offset:256
	global_load_dwordx4 v[166:169], v228, s[10:11] offset:384
	ds_write_b128 v31, v[186:189] offset:512
	ds_write_b128 v0, v[182:185]
	v_add_u32_e32 v229, v241, v228
	global_load_dwordx4 v[186:189], v228, s[10:11] offset:512
	global_load_dwordx4 v[182:185], v229, s[10:11]
	v_mfma_f32_32x32x16_f16 v[2:17], v[102:105], v[68:71], v[2:17]
	v_mfma_f32_32x32x16_f16 v[34:49], v[162:165], v[68:71], v[34:49]
	s_waitcnt lgkmcnt(7)
	v_mfma_f32_32x32x16_f16 v[66:81], v[64:67], v[72:75], 0
	s_waitcnt lgkmcnt(6)
	v_mfma_f32_32x32x16_f16 v[66:81], v[220:223], v[224:227], v[66:81]
	s_setprio 0
